# grid barrier v1 + the per-XCD release words moved 8 KB apart (separate memory channels) inside the zeroed control region
# speedup vs baseline: 1.0023x; 1.0023x over previous
; __device__ __forceinline__ unsigned xb_ld(unsigned* p)              { return __hip_atomic_load(p, __ATOMIC_RELAXED, __HIP_MEMORY_SCOPE_AGENT); }
; __device__ __forceinline__ unsigned xb_add(unsigned* p, unsigned v) { return __hip_atomic_fetch_add(p, v, __ATOMIC_RELAXED, __HIP_MEMORY_SCOPE_AGENT); }
; #define XB_SPIN(cond, bar) do { unsigned _sp = 0; while (cond) { __builtin_amdgcn_s_sleep(1); \
;     if ((++_sp & 255u) == 0u) { if (xb_ld(&(bar)[XB_TMO])) break; if (_sp > XB_SPIN_CAP) { atomicAdd(&(bar)[XB_TMO], 1u); break; } } } } while (0)
; __device__ __forceinline__ void xcd_barrier(const XcdBarrier& b) {
;     ...
;         const unsigned old = xb_add(&bar[XB_XSUB(b.x)], 1u);
;         const unsigned gen = old / nloc;
;         if (old + 1u == (gen + 1u) * nloc) {
;             asm volatile("buffer_inv sc1" ::: "memory");
;             __builtin_amdgcn_fence(__ATOMIC_RELEASE, "agent");
;             asm volatile("s_waitcnt vmcnt(0)" ::: "memory");
;             const unsigned og = xb_add(&bar[XB_TOP], 1u);
;             const unsigned tg = og / nx;
;             if (og + 1u == (tg + 1u) * nx) xb_add(&bar[XB_TOPGEN], 1u);
;             else XB_SPIN(xb_ld(&bar[XB_TOPGEN]) == tg, bar);
;             asm volatile("" ::: "memory");
;             xb_add(&bar[XB_XGEN(b.x)], 1u);
;             asm volatile("" ::: "memory");
;         } else {
;             asm volatile("buffer_inv sc1" ::: "memory");
;             XB_SPIN(xb_ld(&bar[XB_XGEN(b.x)]) == gen, bar);
;             asm volatile("" ::: "memory");
;             asm volatile("s_waitcnt vmcnt(0)" ::: "memory");
;         }
.LBB0_33:
	s_or_b64 exec, exec, s[10:11]
	v_cvt_f32_u32_e32 v5, v3
	s_waitcnt vmcnt(0)
	v_readfirstlane_b32 s0, v4
	v_sub_u32_e32 v4, 0, v3
	v_rcp_iflag_f32_e32 v5, v5
	v_add_u32_e32 v6, s0, v2
	v_mul_f32_e32 v5, 0x4f7ffffe, v5
	v_cvt_u32_f32_e32 v5, v5
	v_mul_lo_u32 v2, v4, v5
	v_mul_hi_u32 v2, v5, v2
	v_add_u32_e32 v2, v5, v2
	v_mul_hi_u32 v2, v6, v2
	v_mul_lo_u32 v4, v2, v3
	v_sub_u32_e32 v4, v6, v4
	v_add_u32_e32 v5, 1, v2
	v_cmp_ge_u32_e32 vcc, v4, v3
	s_nop 1
	v_cndmask_b32_e32 v2, v2, v5, vcc
	v_sub_u32_e32 v5, v4, v3
	v_cndmask_b32_e32 v4, v4, v5, vcc
	v_add_u32_e32 v5, 1, v2
	v_cmp_ge_u32_e32 vcc, v4, v3
	v_add_u32_e32 v4, 1, v6
	s_nop 0
	v_cndmask_b32_e32 v2, v2, v5, vcc
	v_mul_lo_u32 v5, v3, v2
	v_readfirstlane_b32 s98, v2
	v_readlane_b32 s100, v251, 6
	s_lshl_b32 s100, s100, 13
	s_add_u32 s100, s100, s82
	s_addc_u32 s101, s83, 0
	s_add_u32 s100, s100, 0x40000
	s_addc_u32 s101, s101, 0
	v_add_u32_e32 v3, v5, v3
	v_cmp_ne_u32_e32 vcc, v4, v3
	s_and_saveexec_b64 s[0:1], vcc
	s_xor_b64 s[0:1], exec, s[0:1]
	s_cbranch_execz .LBB0_47
	buffer_inv sc1
	v_lshl_add_u32 v2, v2, 1, 1
	s_waitcnt lgkmcnt(0)
	v_mov_b32_e32 v1, 0
	global_load_dword v1, v1, s[100:101] sc1
	s_mov_b32 s14, s100
	s_mov_b32 s15, s101
	s_waitcnt vmcnt(0)
	v_cmp_lt_u32_e32 vcc, v1, v2
	s_and_saveexec_b64 s[10:11], vcc
	s_cbranch_execz .LBB0_46
	s_add_u32 s12, s82, 0x4200
	s_addc_u32 s13, s83, 0
	s_mov_b32 s3, 1
	s_mov_b64 s[16:17], 0
	v_mov_b32_e32 v1, 0
	s_branch .LBB0_37

; __device__ __forceinline__ unsigned xb_ld(unsigned* p)              { return __hip_atomic_load(p, __ATOMIC_RELAXED, __HIP_MEMORY_SCOPE_AGENT); }
; __device__ __forceinline__ unsigned xb_add(unsigned* p, unsigned v) { return __hip_atomic_fetch_add(p, v, __ATOMIC_RELAXED, __HIP_MEMORY_SCOPE_AGENT); }
; #define XB_SPIN(cond, bar) do { unsigned _sp = 0; while (cond) { __builtin_amdgcn_s_sleep(1); \
;     if ((++_sp & 255u) == 0u) { if (xb_ld(&(bar)[XB_TMO])) break; if (_sp > XB_SPIN_CAP) { atomicAdd(&(bar)[XB_TMO], 1u); break; } } } } while (0)
; __device__ __forceinline__ void xcd_barrier(const XcdBarrier& b) {
;     ...
;             asm volatile("buffer_inv sc1" ::: "memory");
;             __builtin_amdgcn_fence(__ATOMIC_RELEASE, "agent");
;             asm volatile("s_waitcnt vmcnt(0)" ::: "memory");
;             const unsigned og = xb_add(&bar[XB_TOP], 1u);
;             const unsigned tg = og / nx;
;             if (og + 1u == (tg + 1u) * nx) xb_add(&bar[XB_TOPGEN], 1u);
;             else XB_SPIN(xb_ld(&bar[XB_TOPGEN]) == tg, bar);
;             asm volatile("" ::: "memory");
;             xb_add(&bar[XB_XGEN(b.x)], 1u);
;             asm volatile("" ::: "memory");
.LBB0_50:
	s_or_b64 exec, exec, s[10:11]
	v_cvt_f32_u32_e32 v4, v1
	s_waitcnt vmcnt(0)
	v_readfirstlane_b32 s0, v3
	s_add_u32 s10, s82, 0x7500
	s_addc_u32 s11, s83, 0
	v_rcp_iflag_f32_e32 v4, v4
	v_add_u32_e32 v2, s0, v2
	v_add_u32_e32 v5, 1, v2
	s_mov_b64 s[12:13], -1
	v_mul_f32_e32 v3, 0x4f7ffffe, v4
	v_cvt_u32_f32_e32 v3, v3
	v_sub_u32_e32 v4, 0, v1
	v_mul_lo_u32 v4, v4, v3
	v_mul_hi_u32 v4, v3, v4
	v_add_u32_e32 v3, v3, v4
	v_mul_hi_u32 v3, v2, v3
	v_mul_lo_u32 v4, v3, v1
	v_sub_u32_e32 v2, v2, v4
	v_add_u32_e32 v6, 1, v3
	v_cmp_ge_u32_e32 vcc, v2, v1
	v_sub_u32_e32 v4, v2, v1
	s_nop 0
	v_cndmask_b32_e32 v3, v3, v6, vcc
	v_cndmask_b32_e32 v2, v2, v4, vcc
	v_add_u32_e32 v4, 1, v3
	v_cmp_ge_u32_e32 vcc, v2, v1
	s_nop 1
	v_cndmask_b32_e32 v4, v3, v4, vcc
	v_mul_lo_u32 v2, v1, v4
	v_add_u32_e32 v1, v2, v1
	v_cmp_ne_u32_e32 vcc, v5, v1
	v_mov_b64_e32 v[2:3], s[10:11]
	s_and_saveexec_b64 s[0:1], vcc
	s_cbranch_execz .LBB0_62
	s_mov_b32 s10, s100
	s_mov_b32 s11, s101
	v_mov_b32_e32 v4, s98
	v_lshl_add_u32 v4, v4, 1, 1
	v_mov_b32_e32 v1, 0
	global_load_dword v2, v1, s[10:11] sc1
	s_mov_b64 s[16:17], 0
	s_waitcnt vmcnt(0)
	v_cmp_lt_u32_e32 vcc, v2, v4
	s_and_saveexec_b64 s[14:15], vcc
	s_cbranch_execz .LBB0_61
	s_add_u32 s12, s82, 0x4200
	s_addc_u32 s13, s83, 0
	s_mov_b32 s3, 1
	s_branch .LBB0_54

; __device__ __forceinline__ unsigned xb_ld(unsigned* p)              { return __hip_atomic_load(p, __ATOMIC_RELAXED, __HIP_MEMORY_SCOPE_AGENT); }
; __device__ __forceinline__ unsigned xb_add(unsigned* p, unsigned v) { return __hip_atomic_fetch_add(p, v, __ATOMIC_RELAXED, __HIP_MEMORY_SCOPE_AGENT); }
; #define XB_SPIN(cond, bar) do { unsigned _sp = 0; while (cond) { __builtin_amdgcn_s_sleep(1); \
;     if ((++_sp & 255u) == 0u) { if (xb_ld(&(bar)[XB_TMO])) break; if (_sp > XB_SPIN_CAP) { atomicAdd(&(bar)[XB_TMO], 1u); break; } } } } while (0)
; __device__ __forceinline__ void xcd_barrier(const XcdBarrier& b) {
;     ...
;             const unsigned og = xb_add(&bar[XB_TOP], 1u);
;             const unsigned tg = og / nx;
;             if (og + 1u == (tg + 1u) * nx) xb_add(&bar[XB_TOPGEN], 1u);
;             else XB_SPIN(xb_ld(&bar[XB_TOPGEN]) == tg, bar);
;             asm volatile("" ::: "memory");
;             xb_add(&bar[XB_XGEN(b.x)], 1u);
.LBB0_62:
	s_or_b64 exec, exec, s[0:1]
	s_and_saveexec_b64 s[0:1], s[12:13]
	s_cbranch_execz .LBB0_64
	v_mov_b32_e32 v1, 1
	global_atomic_add v[2:3], v1, off
	v_mov_b32_e32 v4, 0x40000
	global_atomic_add v4, v1, s[82:83]
	s_nop 0
	v_add_u32_e32 v4, 0x2000, v4
	global_atomic_add v4, v1, s[82:83]
	s_nop 0
	v_add_u32_e32 v4, 0x2000, v4
	global_atomic_add v4, v1, s[82:83]
	s_nop 0
	v_add_u32_e32 v4, 0x2000, v4
	global_atomic_add v4, v1, s[82:83]
	s_nop 0
	v_add_u32_e32 v4, 0x2000, v4
	global_atomic_add v4, v1, s[82:83]
	s_nop 0
	v_add_u32_e32 v4, 0x2000, v4
	global_atomic_add v4, v1, s[82:83]
	s_nop 0
	v_add_u32_e32 v4, 0x2000, v4
	global_atomic_add v4, v1, s[82:83]
	s_nop 0
	v_add_u32_e32 v4, 0x2000, v4
	global_atomic_add v4, v1, s[82:83]
	s_nop 0
	v_add_u32_e32 v4, 0x2000, v4
	global_atomic_add v4, v1, s[82:83]
	s_nop 0
	v_add_u32_e32 v4, 0x2000, v4
	global_atomic_add v4, v1, s[82:83]
	s_nop 0
	v_add_u32_e32 v4, 0x2000, v4
	global_atomic_add v4, v1, s[82:83]
	s_nop 0
	v_add_u32_e32 v4, 0x2000, v4
	global_atomic_add v4, v1, s[82:83]
	s_nop 0
	v_add_u32_e32 v4, 0x2000, v4
	global_atomic_add v4, v1, s[82:83]
	s_nop 0
	v_add_u32_e32 v4, 0x2000, v4
	global_atomic_add v4, v1, s[82:83]
	s_nop 0
	v_add_u32_e32 v4, 0x2000, v4
	global_atomic_add v4, v1, s[82:83]
	s_nop 0
	v_add_u32_e32 v4, 0x2000, v4
	global_atomic_add v4, v1, s[82:83]
.LBB0_64:
	s_or_b64 exec, exec, s[0:1]
	s_mov_b64 s[0:1], exec
	v_mbcnt_lo_u32_b32 v1, s0, 0
	v_mbcnt_hi_u32_b32 v1, s1, v1
	v_cmp_eq_u32_e32 vcc, 0, v1
	s_and_saveexec_b64 s[10:11], vcc
	s_cbranch_execz .LBB0_66
	s_bcnt1_i32_b64 s0, s[0:1]
	v_mov_b32_e32 v1, 0
	v_mov_b32_e32 v2, s0
	global_atomic_add v1, v2, s[100:101]

; __device__ __forceinline__ unsigned xb_ld(unsigned* p)              { return __hip_atomic_load(p, __ATOMIC_RELAXED, __HIP_MEMORY_SCOPE_AGENT); }
; __device__ __forceinline__ unsigned xb_add(unsigned* p, unsigned v) { return __hip_atomic_fetch_add(p, v, __ATOMIC_RELAXED, __HIP_MEMORY_SCOPE_AGENT); }
; #define XB_SPIN(cond, bar) do { unsigned _sp = 0; while (cond) { __builtin_amdgcn_s_sleep(1); \
;     if ((++_sp & 255u) == 0u) { if (xb_ld(&(bar)[XB_TMO])) break; if (_sp > XB_SPIN_CAP) { atomicAdd(&(bar)[XB_TMO], 1u); break; } } } } while (0)
; __device__ __forceinline__ void xcd_barrier(const XcdBarrier& b) {
;     ...
;         const unsigned old = xb_add(&bar[XB_XSUB(b.x)], 1u);
;         const unsigned gen = old / nloc;
;         if (old + 1u == (gen + 1u) * nloc) {
;             asm volatile("buffer_inv sc1" ::: "memory");
;             __builtin_amdgcn_fence(__ATOMIC_RELEASE, "agent");
;             asm volatile("s_waitcnt vmcnt(0)" ::: "memory");
;             const unsigned og = xb_add(&bar[XB_TOP], 1u);
;             const unsigned tg = og / nx;
;             if (og + 1u == (tg + 1u) * nx) xb_add(&bar[XB_TOPGEN], 1u);
;             else XB_SPIN(xb_ld(&bar[XB_TOPGEN]) == tg, bar);
;             asm volatile("" ::: "memory");
;             xb_add(&bar[XB_XGEN(b.x)], 1u);
;             asm volatile("" ::: "memory");
;         } else {
;             asm volatile("buffer_inv sc1" ::: "memory");
;             XB_SPIN(xb_ld(&bar[XB_XGEN(b.x)]) == gen, bar);
;             asm volatile("" ::: "memory");
;             asm volatile("s_waitcnt vmcnt(0)" ::: "memory");
.LBB0_103:
	s_or_b64 exec, exec, s[10:11]
	v_cvt_f32_u32_e32 v5, v3
	s_waitcnt vmcnt(0)
	v_readfirstlane_b32 s3, v4
	v_sub_u32_e32 v4, 0, v3
	v_rcp_iflag_f32_e32 v5, v5
	v_add_u32_e32 v6, s3, v2
	v_mul_f32_e32 v5, 0x4f7ffffe, v5
	v_cvt_u32_f32_e32 v5, v5
	v_mul_lo_u32 v2, v4, v5
	v_mul_hi_u32 v2, v5, v2
	v_add_u32_e32 v2, v5, v2
	v_mul_hi_u32 v2, v6, v2
	v_mul_lo_u32 v4, v2, v3
	v_sub_u32_e32 v4, v6, v4
	v_add_u32_e32 v5, 1, v2
	v_cmp_ge_u32_e32 vcc, v4, v3
	s_nop 1
	v_cndmask_b32_e32 v2, v2, v5, vcc
	v_sub_u32_e32 v5, v4, v3
	v_cndmask_b32_e32 v4, v4, v5, vcc
	v_add_u32_e32 v5, 1, v2
	v_cmp_ge_u32_e32 vcc, v4, v3
	v_add_u32_e32 v4, 1, v6
	s_nop 0
	v_cndmask_b32_e32 v2, v2, v5, vcc
	v_mul_lo_u32 v5, v3, v2
	v_readfirstlane_b32 s98, v2
	v_readlane_b32 s100, v251, 6
	s_lshl_b32 s100, s100, 13
	s_add_u32 s100, s100, s82
	s_addc_u32 s101, s83, 0
	s_add_u32 s100, s100, 0x40000
	s_addc_u32 s101, s101, 0
	v_add_u32_e32 v3, v5, v3
	v_cmp_ne_u32_e32 vcc, v4, v3
	s_and_saveexec_b64 s[8:9], vcc
	s_xor_b64 s[8:9], exec, s[8:9]
	s_cbranch_execz .LBB0_117
	buffer_inv sc1
	v_lshl_add_u32 v2, v2, 1, 1
	s_waitcnt lgkmcnt(0)
	v_mov_b32_e32 v1, 0
	global_load_dword v1, v1, s[100:101] sc1
	s_mov_b32 s14, s100
	s_mov_b32 s15, s101
	s_waitcnt vmcnt(0)
	v_cmp_lt_u32_e32 vcc, v1, v2
	s_and_saveexec_b64 s[10:11], vcc
	s_cbranch_execz .LBB0_116
	s_add_u32 s12, s82, 0x4200
	s_addc_u32 s13, s83, 0
	s_mov_b32 s3, 1
	s_mov_b64 s[16:17], 0
	v_mov_b32_e32 v1, 0
	s_branch .LBB0_107

; __device__ __forceinline__ unsigned xb_ld(unsigned* p)              { return __hip_atomic_load(p, __ATOMIC_RELAXED, __HIP_MEMORY_SCOPE_AGENT); }
; __device__ __forceinline__ unsigned xb_add(unsigned* p, unsigned v) { return __hip_atomic_fetch_add(p, v, __ATOMIC_RELAXED, __HIP_MEMORY_SCOPE_AGENT); }
; #define XB_SPIN(cond, bar) do { unsigned _sp = 0; while (cond) { __builtin_amdgcn_s_sleep(1); \
;     if ((++_sp & 255u) == 0u) { if (xb_ld(&(bar)[XB_TMO])) break; if (_sp > XB_SPIN_CAP) { atomicAdd(&(bar)[XB_TMO], 1u); break; } } } } while (0)
; __device__ __forceinline__ void xcd_barrier(const XcdBarrier& b) {
;     ...
;             const unsigned og = xb_add(&bar[XB_TOP], 1u);
;             const unsigned tg = og / nx;
;             if (og + 1u == (tg + 1u) * nx) xb_add(&bar[XB_TOPGEN], 1u);
;             else XB_SPIN(xb_ld(&bar[XB_TOPGEN]) == tg, bar);
.LBB0_120:
	s_or_b64 exec, exec, s[10:11]
	v_cvt_f32_u32_e32 v4, v1
	s_waitcnt vmcnt(0)
	v_readfirstlane_b32 s3, v3
	s_add_u32 s10, s82, 0x7500
	s_addc_u32 s11, s83, 0
	v_rcp_iflag_f32_e32 v4, v4
	v_add_u32_e32 v2, s3, v2
	v_add_u32_e32 v5, 1, v2
	s_mov_b64 s[12:13], -1
	v_mul_f32_e32 v3, 0x4f7ffffe, v4
	v_cvt_u32_f32_e32 v3, v3
	v_sub_u32_e32 v4, 0, v1
	v_mul_lo_u32 v4, v4, v3
	v_mul_hi_u32 v4, v3, v4
	v_add_u32_e32 v3, v3, v4
	v_mul_hi_u32 v3, v2, v3
	v_mul_lo_u32 v4, v3, v1
	v_sub_u32_e32 v2, v2, v4
	v_add_u32_e32 v6, 1, v3
	v_cmp_ge_u32_e32 vcc, v2, v1
	v_sub_u32_e32 v4, v2, v1
	s_nop 0
	v_cndmask_b32_e32 v3, v3, v6, vcc
	v_cndmask_b32_e32 v2, v2, v4, vcc
	v_add_u32_e32 v4, 1, v3
	v_cmp_ge_u32_e32 vcc, v2, v1
	s_nop 1
	v_cndmask_b32_e32 v4, v3, v4, vcc
	v_mul_lo_u32 v2, v1, v4
	v_add_u32_e32 v1, v2, v1
	v_cmp_ne_u32_e32 vcc, v5, v1
	v_mov_b64_e32 v[2:3], s[10:11]
	s_and_saveexec_b64 s[8:9], vcc
	s_cbranch_execz .LBB0_132
	s_mov_b32 s10, s100
	s_mov_b32 s11, s101
	v_mov_b32_e32 v4, s98
	v_lshl_add_u32 v4, v4, 1, 1
	v_mov_b32_e32 v1, 0
	global_load_dword v2, v1, s[10:11] sc1
	s_mov_b64 s[16:17], 0
	s_waitcnt vmcnt(0)
	v_cmp_lt_u32_e32 vcc, v2, v4
	s_and_saveexec_b64 s[14:15], vcc
	s_cbranch_execz .LBB0_131
	s_add_u32 s12, s82, 0x4200
	s_addc_u32 s13, s83, 0
	s_mov_b32 s3, 1
	s_branch .LBB0_124

; __device__ __forceinline__ unsigned xb_ld(unsigned* p)              { return __hip_atomic_load(p, __ATOMIC_RELAXED, __HIP_MEMORY_SCOPE_AGENT); }
; __device__ __forceinline__ unsigned xb_add(unsigned* p, unsigned v) { return __hip_atomic_fetch_add(p, v, __ATOMIC_RELAXED, __HIP_MEMORY_SCOPE_AGENT); }
; #define XB_SPIN(cond, bar) do { unsigned _sp = 0; while (cond) { __builtin_amdgcn_s_sleep(1); \
;     if ((++_sp & 255u) == 0u) { if (xb_ld(&(bar)[XB_TMO])) break; if (_sp > XB_SPIN_CAP) { atomicAdd(&(bar)[XB_TMO], 1u); break; } } } } while (0)
; __device__ __forceinline__ void xcd_barrier(const XcdBarrier& b) {
;     ...
;             if (og + 1u == (tg + 1u) * nx) xb_add(&bar[XB_TOPGEN], 1u);
;             else XB_SPIN(xb_ld(&bar[XB_TOPGEN]) == tg, bar);
;             asm volatile("" ::: "memory");
;             xb_add(&bar[XB_XGEN(b.x)], 1u);
;             asm volatile("" ::: "memory");
.LBB0_132:
	s_or_b64 exec, exec, s[8:9]
	s_and_saveexec_b64 s[8:9], s[12:13]
	s_cbranch_execz .LBB0_134
	v_mov_b32_e32 v1, 1
	global_atomic_add v[2:3], v1, off
	v_mov_b32_e32 v4, 0x40000
	global_atomic_add v4, v1, s[82:83]
	s_nop 0
	v_add_u32_e32 v4, 0x2000, v4
	global_atomic_add v4, v1, s[82:83]
	s_nop 0
	v_add_u32_e32 v4, 0x2000, v4
	global_atomic_add v4, v1, s[82:83]
	s_nop 0
	v_add_u32_e32 v4, 0x2000, v4
	global_atomic_add v4, v1, s[82:83]
	s_nop 0
	v_add_u32_e32 v4, 0x2000, v4
	global_atomic_add v4, v1, s[82:83]
	s_nop 0
	v_add_u32_e32 v4, 0x2000, v4
	global_atomic_add v4, v1, s[82:83]
	s_nop 0
	v_add_u32_e32 v4, 0x2000, v4
	global_atomic_add v4, v1, s[82:83]
	s_nop 0
	v_add_u32_e32 v4, 0x2000, v4
	global_atomic_add v4, v1, s[82:83]
	s_nop 0
	v_add_u32_e32 v4, 0x2000, v4
	global_atomic_add v4, v1, s[82:83]
	s_nop 0
	v_add_u32_e32 v4, 0x2000, v4
	global_atomic_add v4, v1, s[82:83]
	s_nop 0
	v_add_u32_e32 v4, 0x2000, v4
	global_atomic_add v4, v1, s[82:83]
	s_nop 0
	v_add_u32_e32 v4, 0x2000, v4
	global_atomic_add v4, v1, s[82:83]
	s_nop 0
	v_add_u32_e32 v4, 0x2000, v4
	global_atomic_add v4, v1, s[82:83]
	s_nop 0
	v_add_u32_e32 v4, 0x2000, v4
	global_atomic_add v4, v1, s[82:83]
	s_nop 0
	v_add_u32_e32 v4, 0x2000, v4
	global_atomic_add v4, v1, s[82:83]
	s_nop 0
	v_add_u32_e32 v4, 0x2000, v4
	global_atomic_add v4, v1, s[82:83]
.LBB0_134:
	s_or_b64 exec, exec, s[8:9]
	s_mov_b64 s[8:9], exec
	v_mbcnt_lo_u32_b32 v1, s8, 0
	v_mbcnt_hi_u32_b32 v1, s9, v1
	v_cmp_eq_u32_e32 vcc, 0, v1
	s_and_saveexec_b64 s[10:11], vcc
	s_cbranch_execz .LBB0_136
	s_bcnt1_i32_b64 s3, s[8:9]
	v_mov_b32_e32 v1, 0
	v_mov_b32_e32 v2, s3
	global_atomic_add v1, v2, s[100:101]

; __device__ __forceinline__ unsigned xb_ld(unsigned* p)              { return __hip_atomic_load(p, __ATOMIC_RELAXED, __HIP_MEMORY_SCOPE_AGENT); }
; __device__ __forceinline__ unsigned xb_add(unsigned* p, unsigned v) { return __hip_atomic_fetch_add(p, v, __ATOMIC_RELAXED, __HIP_MEMORY_SCOPE_AGENT); }
; #define XB_SPIN(cond, bar) do { unsigned _sp = 0; while (cond) { __builtin_amdgcn_s_sleep(1); \
;     if ((++_sp & 255u) == 0u) { if (xb_ld(&(bar)[XB_TMO])) break; if (_sp > XB_SPIN_CAP) { atomicAdd(&(bar)[XB_TMO], 1u); break; } } } } while (0)
; __device__ __forceinline__ void xcd_barrier(const XcdBarrier& b) {
;     ...
;         const unsigned old = xb_add(&bar[XB_XSUB(b.x)], 1u);
;         const unsigned gen = old / nloc;
;         if (old + 1u == (gen + 1u) * nloc) {
;             asm volatile("buffer_inv sc1" ::: "memory");
;             __builtin_amdgcn_fence(__ATOMIC_RELEASE, "agent");
;             asm volatile("s_waitcnt vmcnt(0)" ::: "memory");
;             const unsigned og = xb_add(&bar[XB_TOP], 1u);
;             const unsigned tg = og / nx;
;             if (og + 1u == (tg + 1u) * nx) xb_add(&bar[XB_TOPGEN], 1u);
;             else XB_SPIN(xb_ld(&bar[XB_TOPGEN]) == tg, bar);
;             asm volatile("" ::: "memory");
;             xb_add(&bar[XB_XGEN(b.x)], 1u);
;             asm volatile("" ::: "memory");
;         } else {
;             asm volatile("buffer_inv sc1" ::: "memory");
;             XB_SPIN(xb_ld(&bar[XB_XGEN(b.x)]) == gen, bar);
;             asm volatile("" ::: "memory");
;             asm volatile("s_waitcnt vmcnt(0)" ::: "memory");
.LBB0_183:
	s_or_b64 exec, exec, s[10:11]
	v_cvt_f32_u32_e32 v5, v3
	s_waitcnt vmcnt(0)
	v_readfirstlane_b32 s8, v4
	v_sub_u32_e32 v4, 0, v3
	v_rcp_iflag_f32_e32 v5, v5
	v_add_u32_e32 v6, s8, v2
	v_mul_f32_e32 v5, 0x4f7ffffe, v5
	v_cvt_u32_f32_e32 v5, v5
	v_mul_lo_u32 v2, v4, v5
	v_mul_hi_u32 v2, v5, v2
	v_add_u32_e32 v2, v5, v2
	v_mul_hi_u32 v2, v6, v2
	v_mul_lo_u32 v4, v2, v3
	v_sub_u32_e32 v4, v6, v4
	v_add_u32_e32 v5, 1, v2
	v_cmp_ge_u32_e32 vcc, v4, v3
	s_nop 1
	v_cndmask_b32_e32 v2, v2, v5, vcc
	v_sub_u32_e32 v5, v4, v3
	v_cndmask_b32_e32 v4, v4, v5, vcc
	v_add_u32_e32 v5, 1, v2
	v_cmp_ge_u32_e32 vcc, v4, v3
	v_add_u32_e32 v4, 1, v6
	s_nop 0
	v_cndmask_b32_e32 v2, v2, v5, vcc
	v_mul_lo_u32 v5, v3, v2
	v_readfirstlane_b32 s98, v2
	v_readlane_b32 s100, v251, 6
	s_lshl_b32 s100, s100, 13
	s_add_u32 s100, s100, s82
	s_addc_u32 s101, s83, 0
	s_add_u32 s100, s100, 0x40000
	s_addc_u32 s101, s101, 0
	v_add_u32_e32 v3, v5, v3
	v_cmp_ne_u32_e32 vcc, v4, v3
	s_and_saveexec_b64 s[8:9], vcc
	s_xor_b64 s[8:9], exec, s[8:9]
	s_cbranch_execz .LBB0_197
	buffer_inv sc1
	v_lshl_add_u32 v2, v2, 1, 1
	s_waitcnt lgkmcnt(0)
	v_mov_b32_e32 v1, 0
	global_load_dword v1, v1, s[100:101] sc1
	s_mov_b32 s16, s100
	s_mov_b32 s17, s101
	s_waitcnt vmcnt(0)
	v_cmp_lt_u32_e32 vcc, v1, v2
	s_and_saveexec_b64 s[10:11], vcc
	s_cbranch_execz .LBB0_196
	s_add_u32 s14, s82, 0x4200
	s_addc_u32 s15, s83, 0
	s_mov_b32 s28, 1
	s_mov_b64 s[18:19], 0
	v_mov_b32_e32 v1, 0
	s_branch .LBB0_187

; __device__ __forceinline__ unsigned xb_ld(unsigned* p)              { return __hip_atomic_load(p, __ATOMIC_RELAXED, __HIP_MEMORY_SCOPE_AGENT); }
; __device__ __forceinline__ unsigned xb_add(unsigned* p, unsigned v) { return __hip_atomic_fetch_add(p, v, __ATOMIC_RELAXED, __HIP_MEMORY_SCOPE_AGENT); }
; #define XB_SPIN(cond, bar) do { unsigned _sp = 0; while (cond) { __builtin_amdgcn_s_sleep(1); \
;     if ((++_sp & 255u) == 0u) { if (xb_ld(&(bar)[XB_TMO])) break; if (_sp > XB_SPIN_CAP) { atomicAdd(&(bar)[XB_TMO], 1u); break; } } } } while (0)
; __device__ __forceinline__ void xcd_barrier(const XcdBarrier& b) {
;     ...
;             const unsigned og = xb_add(&bar[XB_TOP], 1u);
;             const unsigned tg = og / nx;
;             if (og + 1u == (tg + 1u) * nx) xb_add(&bar[XB_TOPGEN], 1u);
;             else XB_SPIN(xb_ld(&bar[XB_TOPGEN]) == tg, bar);
.LBB0_200:
	s_or_b64 exec, exec, s[10:11]
	v_cvt_f32_u32_e32 v4, v1
	s_waitcnt vmcnt(0)
	v_readfirstlane_b32 s8, v3
	s_add_u32 s10, s82, 0x7500
	s_addc_u32 s11, s83, 0
	v_rcp_iflag_f32_e32 v4, v4
	v_add_u32_e32 v2, s8, v2
	v_add_u32_e32 v5, 1, v2
	s_mov_b64 s[14:15], -1
	v_mul_f32_e32 v3, 0x4f7ffffe, v4
	v_cvt_u32_f32_e32 v3, v3
	v_sub_u32_e32 v4, 0, v1
	v_mul_lo_u32 v4, v4, v3
	v_mul_hi_u32 v4, v3, v4
	v_add_u32_e32 v3, v3, v4
	v_mul_hi_u32 v3, v2, v3
	v_mul_lo_u32 v4, v3, v1
	v_sub_u32_e32 v2, v2, v4
	v_add_u32_e32 v6, 1, v3
	v_cmp_ge_u32_e32 vcc, v2, v1
	v_sub_u32_e32 v4, v2, v1
	s_nop 0
	v_cndmask_b32_e32 v3, v3, v6, vcc
	v_cndmask_b32_e32 v2, v2, v4, vcc
	v_add_u32_e32 v4, 1, v3
	v_cmp_ge_u32_e32 vcc, v2, v1
	s_nop 1
	v_cndmask_b32_e32 v4, v3, v4, vcc
	v_mul_lo_u32 v2, v1, v4
	v_add_u32_e32 v1, v2, v1
	v_cmp_ne_u32_e32 vcc, v5, v1
	v_mov_b64_e32 v[2:3], s[10:11]
	s_and_saveexec_b64 s[8:9], vcc
	s_cbranch_execz .LBB0_212
	s_mov_b32 s10, s100
	s_mov_b32 s11, s101
	v_mov_b32_e32 v4, s98
	v_lshl_add_u32 v4, v4, 1, 1
	v_mov_b32_e32 v1, 0
	global_load_dword v2, v1, s[10:11] sc1
	s_mov_b64 s[18:19], 0
	s_waitcnt vmcnt(0)
	v_cmp_lt_u32_e32 vcc, v2, v4
	s_and_saveexec_b64 s[16:17], vcc
	s_cbranch_execz .LBB0_211
	s_add_u32 s14, s82, 0x4200
	s_addc_u32 s15, s83, 0
	s_mov_b32 s28, 1
	s_branch .LBB0_204

; __device__ __forceinline__ unsigned xb_ld(unsigned* p)              { return __hip_atomic_load(p, __ATOMIC_RELAXED, __HIP_MEMORY_SCOPE_AGENT); }
; __device__ __forceinline__ unsigned xb_add(unsigned* p, unsigned v) { return __hip_atomic_fetch_add(p, v, __ATOMIC_RELAXED, __HIP_MEMORY_SCOPE_AGENT); }
; #define XB_SPIN(cond, bar) do { unsigned _sp = 0; while (cond) { __builtin_amdgcn_s_sleep(1); \
;     if ((++_sp & 255u) == 0u) { if (xb_ld(&(bar)[XB_TMO])) break; if (_sp > XB_SPIN_CAP) { atomicAdd(&(bar)[XB_TMO], 1u); break; } } } } while (0)
; __device__ __forceinline__ void xcd_barrier(const XcdBarrier& b) {
;     ...
;             if (og + 1u == (tg + 1u) * nx) xb_add(&bar[XB_TOPGEN], 1u);
;             else XB_SPIN(xb_ld(&bar[XB_TOPGEN]) == tg, bar);
;             asm volatile("" ::: "memory");
;             xb_add(&bar[XB_XGEN(b.x)], 1u);
;             asm volatile("" ::: "memory");
.LBB0_212:
	s_or_b64 exec, exec, s[8:9]
	s_and_saveexec_b64 s[8:9], s[14:15]
	s_cbranch_execz .LBB0_214
	v_mov_b32_e32 v1, 1
	global_atomic_add v[2:3], v1, off
	v_mov_b32_e32 v4, 0x40000
	global_atomic_add v4, v1, s[82:83]
	s_nop 0
	v_add_u32_e32 v4, 0x2000, v4
	global_atomic_add v4, v1, s[82:83]
	s_nop 0
	v_add_u32_e32 v4, 0x2000, v4
	global_atomic_add v4, v1, s[82:83]
	s_nop 0
	v_add_u32_e32 v4, 0x2000, v4
	global_atomic_add v4, v1, s[82:83]
	s_nop 0
	v_add_u32_e32 v4, 0x2000, v4
	global_atomic_add v4, v1, s[82:83]
	s_nop 0
	v_add_u32_e32 v4, 0x2000, v4
	global_atomic_add v4, v1, s[82:83]
	s_nop 0
	v_add_u32_e32 v4, 0x2000, v4
	global_atomic_add v4, v1, s[82:83]
	s_nop 0
	v_add_u32_e32 v4, 0x2000, v4
	global_atomic_add v4, v1, s[82:83]
	s_nop 0
	v_add_u32_e32 v4, 0x2000, v4
	global_atomic_add v4, v1, s[82:83]
	s_nop 0
	v_add_u32_e32 v4, 0x2000, v4
	global_atomic_add v4, v1, s[82:83]
	s_nop 0
	v_add_u32_e32 v4, 0x2000, v4
	global_atomic_add v4, v1, s[82:83]
	s_nop 0
	v_add_u32_e32 v4, 0x2000, v4
	global_atomic_add v4, v1, s[82:83]
	s_nop 0
	v_add_u32_e32 v4, 0x2000, v4
	global_atomic_add v4, v1, s[82:83]
	s_nop 0
	v_add_u32_e32 v4, 0x2000, v4
	global_atomic_add v4, v1, s[82:83]
	s_nop 0
	v_add_u32_e32 v4, 0x2000, v4
	global_atomic_add v4, v1, s[82:83]
	s_nop 0
	v_add_u32_e32 v4, 0x2000, v4
	global_atomic_add v4, v1, s[82:83]
.LBB0_214:
	s_or_b64 exec, exec, s[8:9]
	s_mov_b64 s[8:9], exec
	v_mbcnt_lo_u32_b32 v1, s8, 0
	v_mbcnt_hi_u32_b32 v1, s9, v1
	v_cmp_eq_u32_e32 vcc, 0, v1
	s_and_saveexec_b64 s[10:11], vcc
	s_cbranch_execz .LBB0_216
	s_bcnt1_i32_b64 s8, s[8:9]
	v_mov_b32_e32 v1, 0
	v_mov_b32_e32 v2, s8
	global_atomic_add v1, v2, s[100:101]

; __device__ __forceinline__ unsigned xb_ld(unsigned* p)              { return __hip_atomic_load(p, __ATOMIC_RELAXED, __HIP_MEMORY_SCOPE_AGENT); }
; __device__ __forceinline__ unsigned xb_add(unsigned* p, unsigned v) { return __hip_atomic_fetch_add(p, v, __ATOMIC_RELAXED, __HIP_MEMORY_SCOPE_AGENT); }
; #define XB_SPIN(cond, bar) do { unsigned _sp = 0; while (cond) { __builtin_amdgcn_s_sleep(1); \
;     if ((++_sp & 255u) == 0u) { if (xb_ld(&(bar)[XB_TMO])) break; if (_sp > XB_SPIN_CAP) { atomicAdd(&(bar)[XB_TMO], 1u); break; } } } } while (0)
; __device__ __forceinline__ void xcd_barrier(const XcdBarrier& b) {
;     ...
;         const unsigned old = xb_add(&bar[XB_XSUB(b.x)], 1u);
;         const unsigned gen = old / nloc;
;         if (old + 1u == (gen + 1u) * nloc) {
;             asm volatile("buffer_inv sc1" ::: "memory");
;             __builtin_amdgcn_fence(__ATOMIC_RELEASE, "agent");
;             asm volatile("s_waitcnt vmcnt(0)" ::: "memory");
;             const unsigned og = xb_add(&bar[XB_TOP], 1u);
;             const unsigned tg = og / nx;
;             if (og + 1u == (tg + 1u) * nx) xb_add(&bar[XB_TOPGEN], 1u);
;             else XB_SPIN(xb_ld(&bar[XB_TOPGEN]) == tg, bar);
;             asm volatile("" ::: "memory");
;             xb_add(&bar[XB_XGEN(b.x)], 1u);
;             asm volatile("" ::: "memory");
;         } else {
;             asm volatile("buffer_inv sc1" ::: "memory");
;             XB_SPIN(xb_ld(&bar[XB_XGEN(b.x)]) == gen, bar);
;             asm volatile("" ::: "memory");
;             asm volatile("s_waitcnt vmcnt(0)" ::: "memory");
.LBB0_626:
	s_or_b64 exec, exec, s[10:11]
	v_cvt_f32_u32_e32 v5, v3
	s_waitcnt vmcnt(0)
	v_readfirstlane_b32 s8, v4
	v_sub_u32_e32 v4, 0, v3
	v_rcp_iflag_f32_e32 v5, v5
	v_add_u32_e32 v6, s8, v2
	v_mul_f32_e32 v5, 0x4f7ffffe, v5
	v_cvt_u32_f32_e32 v5, v5
	v_mul_lo_u32 v2, v4, v5
	v_mul_hi_u32 v2, v5, v2
	v_add_u32_e32 v2, v5, v2
	v_mul_hi_u32 v2, v6, v2
	v_mul_lo_u32 v4, v2, v3
	v_sub_u32_e32 v4, v6, v4
	v_add_u32_e32 v5, 1, v2
	v_cmp_ge_u32_e32 vcc, v4, v3
	s_nop 1
	v_cndmask_b32_e32 v2, v2, v5, vcc
	v_sub_u32_e32 v5, v4, v3
	v_cndmask_b32_e32 v4, v4, v5, vcc
	v_add_u32_e32 v5, 1, v2
	v_cmp_ge_u32_e32 vcc, v4, v3
	v_add_u32_e32 v4, 1, v6
	s_nop 0
	v_cndmask_b32_e32 v2, v2, v5, vcc
	v_mul_lo_u32 v5, v3, v2
	v_readfirstlane_b32 s98, v2
	v_readlane_b32 s100, v251, 6
	s_lshl_b32 s100, s100, 13
	s_add_u32 s100, s100, s82
	s_addc_u32 s101, s83, 0
	s_add_u32 s100, s100, 0x40000
	s_addc_u32 s101, s101, 0
	v_add_u32_e32 v3, v5, v3
	v_cmp_ne_u32_e32 vcc, v4, v3
	s_and_saveexec_b64 s[8:9], vcc
	s_xor_b64 s[8:9], exec, s[8:9]
	s_cbranch_execz .LBB0_640
	buffer_inv sc1
	v_lshl_add_u32 v2, v2, 1, 1
	s_waitcnt lgkmcnt(0)
	v_mov_b32_e32 v1, 0
	global_load_dword v1, v1, s[100:101] sc1
	s_mov_b32 s14, s100
	s_mov_b32 s15, s101
	s_waitcnt vmcnt(0)
	v_cmp_lt_u32_e32 vcc, v1, v2
	s_and_saveexec_b64 s[10:11], vcc
	s_cbranch_execz .LBB0_639
	s_add_u32 s12, s82, 0x4200
	s_addc_u32 s13, s83, 0
	s_mov_b32 s26, 1
	s_mov_b64 s[16:17], 0
	v_mov_b32_e32 v1, 0
	s_branch .LBB0_630

; __device__ __forceinline__ unsigned xb_ld(unsigned* p)              { return __hip_atomic_load(p, __ATOMIC_RELAXED, __HIP_MEMORY_SCOPE_AGENT); }
; __device__ __forceinline__ unsigned xb_add(unsigned* p, unsigned v) { return __hip_atomic_fetch_add(p, v, __ATOMIC_RELAXED, __HIP_MEMORY_SCOPE_AGENT); }
; #define XB_SPIN(cond, bar) do { unsigned _sp = 0; while (cond) { __builtin_amdgcn_s_sleep(1); \
;     if ((++_sp & 255u) == 0u) { if (xb_ld(&(bar)[XB_TMO])) break; if (_sp > XB_SPIN_CAP) { atomicAdd(&(bar)[XB_TMO], 1u); break; } } } } while (0)
; __device__ __forceinline__ void xcd_barrier(const XcdBarrier& b) {
;     ...
;             const unsigned og = xb_add(&bar[XB_TOP], 1u);
;             const unsigned tg = og / nx;
;             if (og + 1u == (tg + 1u) * nx) xb_add(&bar[XB_TOPGEN], 1u);
;             else XB_SPIN(xb_ld(&bar[XB_TOPGEN]) == tg, bar);
.LBB0_643:
	s_or_b64 exec, exec, s[10:11]
	v_cvt_f32_u32_e32 v4, v1
	s_waitcnt vmcnt(0)
	v_readfirstlane_b32 s8, v3
	s_add_u32 s10, s82, 0x7500
	s_addc_u32 s11, s83, 0
	v_rcp_iflag_f32_e32 v4, v4
	v_add_u32_e32 v2, s8, v2
	v_add_u32_e32 v5, 1, v2
	s_mov_b64 s[12:13], -1
	v_mul_f32_e32 v3, 0x4f7ffffe, v4
	v_cvt_u32_f32_e32 v3, v3
	v_sub_u32_e32 v4, 0, v1
	v_mul_lo_u32 v4, v4, v3
	v_mul_hi_u32 v4, v3, v4
	v_add_u32_e32 v3, v3, v4
	v_mul_hi_u32 v3, v2, v3
	v_mul_lo_u32 v4, v3, v1
	v_sub_u32_e32 v2, v2, v4
	v_add_u32_e32 v6, 1, v3
	v_cmp_ge_u32_e32 vcc, v2, v1
	v_sub_u32_e32 v4, v2, v1
	s_nop 0
	v_cndmask_b32_e32 v3, v3, v6, vcc
	v_cndmask_b32_e32 v2, v2, v4, vcc
	v_add_u32_e32 v4, 1, v3
	v_cmp_ge_u32_e32 vcc, v2, v1
	s_nop 1
	v_cndmask_b32_e32 v4, v3, v4, vcc
	v_mul_lo_u32 v2, v1, v4
	v_add_u32_e32 v1, v2, v1
	v_cmp_ne_u32_e32 vcc, v5, v1
	v_mov_b64_e32 v[2:3], s[10:11]
	s_and_saveexec_b64 s[8:9], vcc
	s_cbranch_execz .LBB0_655
	s_mov_b32 s10, s100
	s_mov_b32 s11, s101
	v_mov_b32_e32 v4, s98
	v_lshl_add_u32 v4, v4, 1, 1
	v_mov_b32_e32 v1, 0
	global_load_dword v2, v1, s[10:11] sc1
	s_mov_b64 s[16:17], 0
	s_waitcnt vmcnt(0)
	v_cmp_lt_u32_e32 vcc, v2, v4
	s_and_saveexec_b64 s[14:15], vcc
	s_cbranch_execz .LBB0_654
	s_add_u32 s12, s82, 0x4200
	s_addc_u32 s13, s83, 0
	s_mov_b32 s26, 1
	s_branch .LBB0_647

; __device__ __forceinline__ unsigned xb_ld(unsigned* p)              { return __hip_atomic_load(p, __ATOMIC_RELAXED, __HIP_MEMORY_SCOPE_AGENT); }
; __device__ __forceinline__ unsigned xb_add(unsigned* p, unsigned v) { return __hip_atomic_fetch_add(p, v, __ATOMIC_RELAXED, __HIP_MEMORY_SCOPE_AGENT); }
; #define XB_SPIN(cond, bar) do { unsigned _sp = 0; while (cond) { __builtin_amdgcn_s_sleep(1); \
;     if ((++_sp & 255u) == 0u) { if (xb_ld(&(bar)[XB_TMO])) break; if (_sp > XB_SPIN_CAP) { atomicAdd(&(bar)[XB_TMO], 1u); break; } } } } while (0)
; __device__ __forceinline__ void xcd_barrier(const XcdBarrier& b) {
;     ...
;         const unsigned old = xb_add(&bar[XB_XSUB(b.x)], 1u);
;         const unsigned gen = old / nloc;
;         if (old + 1u == (gen + 1u) * nloc) {
;             asm volatile("buffer_inv sc1" ::: "memory");
;             __builtin_amdgcn_fence(__ATOMIC_RELEASE, "agent");
;             asm volatile("s_waitcnt vmcnt(0)" ::: "memory");
;             const unsigned og = xb_add(&bar[XB_TOP], 1u);
;             const unsigned tg = og / nx;
;             if (og + 1u == (tg + 1u) * nx) xb_add(&bar[XB_TOPGEN], 1u);
;             else XB_SPIN(xb_ld(&bar[XB_TOPGEN]) == tg, bar);
;             asm volatile("" ::: "memory");
;             xb_add(&bar[XB_XGEN(b.x)], 1u);
;             asm volatile("" ::: "memory");
;         } else {
;             asm volatile("buffer_inv sc1" ::: "memory");
;             XB_SPIN(xb_ld(&bar[XB_XGEN(b.x)]) == gen, bar);
;             asm volatile("" ::: "memory");
;             asm volatile("s_waitcnt vmcnt(0)" ::: "memory");
.LBB0_1020:
	s_or_b64 exec, exec, s[12:13]
	v_cvt_f32_u32_e32 v5, v3
	s_waitcnt vmcnt(0)
	v_readfirstlane_b32 s10, v4
	v_sub_u32_e32 v4, 0, v3
	v_rcp_iflag_f32_e32 v5, v5
	v_add_u32_e32 v6, s10, v2
	v_mul_f32_e32 v5, 0x4f7ffffe, v5
	v_cvt_u32_f32_e32 v5, v5
	v_mul_lo_u32 v2, v4, v5
	v_mul_hi_u32 v2, v5, v2
	v_add_u32_e32 v2, v5, v2
	v_mul_hi_u32 v2, v6, v2
	v_mul_lo_u32 v4, v2, v3
	v_sub_u32_e32 v4, v6, v4
	v_add_u32_e32 v5, 1, v2
	v_cmp_ge_u32_e32 vcc, v4, v3
	s_nop 1
	v_cndmask_b32_e32 v2, v2, v5, vcc
	v_sub_u32_e32 v5, v4, v3
	v_cndmask_b32_e32 v4, v4, v5, vcc
	v_add_u32_e32 v5, 1, v2
	v_cmp_ge_u32_e32 vcc, v4, v3
	v_add_u32_e32 v4, 1, v6
	s_nop 0
	v_cndmask_b32_e32 v2, v2, v5, vcc
	v_mul_lo_u32 v5, v3, v2
	v_readfirstlane_b32 s98, v2
	v_readlane_b32 s100, v251, 6
	s_lshl_b32 s100, s100, 13
	s_add_u32 s100, s100, s82
	s_addc_u32 s101, s83, 0
	s_add_u32 s100, s100, 0x40000
	s_addc_u32 s101, s101, 0
	v_add_u32_e32 v3, v5, v3
	v_cmp_ne_u32_e32 vcc, v4, v3
	s_and_saveexec_b64 s[10:11], vcc
	s_xor_b64 s[10:11], exec, s[10:11]
	s_cbranch_execz .LBB0_1034
	buffer_inv sc1
	v_lshl_add_u32 v2, v2, 1, 1
	s_waitcnt lgkmcnt(0)
	v_mov_b32_e32 v1, 0
	global_load_dword v1, v1, s[100:101] sc1
	s_mov_b32 s16, s100
	s_mov_b32 s17, s101
	s_waitcnt vmcnt(0)
	v_cmp_lt_u32_e32 vcc, v1, v2
	s_and_saveexec_b64 s[12:13], vcc
	s_cbranch_execz .LBB0_1033
	s_add_u32 s14, s82, 0x4200
	s_addc_u32 s15, s83, 0
	s_mov_b32 s28, 1
	s_mov_b64 s[18:19], 0
	v_mov_b32_e32 v1, 0
	s_branch .LBB0_1024

; __device__ __forceinline__ unsigned xb_ld(unsigned* p)              { return __hip_atomic_load(p, __ATOMIC_RELAXED, __HIP_MEMORY_SCOPE_AGENT); }
; __device__ __forceinline__ unsigned xb_add(unsigned* p, unsigned v) { return __hip_atomic_fetch_add(p, v, __ATOMIC_RELAXED, __HIP_MEMORY_SCOPE_AGENT); }
; #define XB_SPIN(cond, bar) do { unsigned _sp = 0; while (cond) { __builtin_amdgcn_s_sleep(1); \
;     if ((++_sp & 255u) == 0u) { if (xb_ld(&(bar)[XB_TMO])) break; if (_sp > XB_SPIN_CAP) { atomicAdd(&(bar)[XB_TMO], 1u); break; } } } } while (0)
; __device__ __forceinline__ void xcd_barrier(const XcdBarrier& b) {
;     ...
;             const unsigned og = xb_add(&bar[XB_TOP], 1u);
;             const unsigned tg = og / nx;
;             if (og + 1u == (tg + 1u) * nx) xb_add(&bar[XB_TOPGEN], 1u);
;             else XB_SPIN(xb_ld(&bar[XB_TOPGEN]) == tg, bar);
.LBB0_1037:
	s_or_b64 exec, exec, s[12:13]
	v_cvt_f32_u32_e32 v4, v1
	s_waitcnt vmcnt(0)
	v_readfirstlane_b32 s10, v3
	s_add_u32 s12, s82, 0x7500
	s_addc_u32 s13, s83, 0
	v_rcp_iflag_f32_e32 v4, v4
	v_add_u32_e32 v2, s10, v2
	v_add_u32_e32 v5, 1, v2
	s_mov_b64 s[14:15], -1
	v_mul_f32_e32 v3, 0x4f7ffffe, v4
	v_cvt_u32_f32_e32 v3, v3
	v_sub_u32_e32 v4, 0, v1
	v_mul_lo_u32 v4, v4, v3
	v_mul_hi_u32 v4, v3, v4
	v_add_u32_e32 v3, v3, v4
	v_mul_hi_u32 v3, v2, v3
	v_mul_lo_u32 v4, v3, v1
	v_sub_u32_e32 v2, v2, v4
	v_add_u32_e32 v6, 1, v3
	v_cmp_ge_u32_e32 vcc, v2, v1
	v_sub_u32_e32 v4, v2, v1
	s_nop 0
	v_cndmask_b32_e32 v3, v3, v6, vcc
	v_cndmask_b32_e32 v2, v2, v4, vcc
	v_add_u32_e32 v4, 1, v3
	v_cmp_ge_u32_e32 vcc, v2, v1
	s_nop 1
	v_cndmask_b32_e32 v4, v3, v4, vcc
	v_mul_lo_u32 v2, v1, v4
	v_add_u32_e32 v1, v2, v1
	v_cmp_ne_u32_e32 vcc, v5, v1
	v_mov_b64_e32 v[2:3], s[12:13]
	s_and_saveexec_b64 s[10:11], vcc
	s_cbranch_execz .LBB0_1049
	s_mov_b32 s12, s100
	s_mov_b32 s13, s101
	v_mov_b32_e32 v4, s98
	v_lshl_add_u32 v4, v4, 1, 1
	v_mov_b32_e32 v1, 0
	global_load_dword v2, v1, s[12:13] sc1
	s_mov_b64 s[18:19], 0
	s_waitcnt vmcnt(0)
	v_cmp_lt_u32_e32 vcc, v2, v4
	s_and_saveexec_b64 s[16:17], vcc
	s_cbranch_execz .LBB0_1048
	s_add_u32 s14, s82, 0x4200
	s_addc_u32 s15, s83, 0
	s_mov_b32 s28, 1
	s_branch .LBB0_1041

; __device__ __forceinline__ unsigned xb_ld(unsigned* p)              { return __hip_atomic_load(p, __ATOMIC_RELAXED, __HIP_MEMORY_SCOPE_AGENT); }
; __device__ __forceinline__ unsigned xb_add(unsigned* p, unsigned v) { return __hip_atomic_fetch_add(p, v, __ATOMIC_RELAXED, __HIP_MEMORY_SCOPE_AGENT); }
; #define XB_SPIN(cond, bar) do { unsigned _sp = 0; while (cond) { __builtin_amdgcn_s_sleep(1); \
;     if ((++_sp & 255u) == 0u) { if (xb_ld(&(bar)[XB_TMO])) break; if (_sp > XB_SPIN_CAP) { atomicAdd(&(bar)[XB_TMO], 1u); break; } } } } while (0)
; __device__ __forceinline__ void xcd_barrier(const XcdBarrier& b) {
;     ...
;             if (og + 1u == (tg + 1u) * nx) xb_add(&bar[XB_TOPGEN], 1u);
;             else XB_SPIN(xb_ld(&bar[XB_TOPGEN]) == tg, bar);
;             asm volatile("" ::: "memory");
;             xb_add(&bar[XB_XGEN(b.x)], 1u);
;             asm volatile("" ::: "memory");
.LBB0_1049:
	s_or_b64 exec, exec, s[10:11]
	s_and_saveexec_b64 s[10:11], s[14:15]
	s_cbranch_execz .LBB0_1051
	v_mov_b32_e32 v1, 1
	global_atomic_add v[2:3], v1, off
	v_mov_b32_e32 v4, 0x40000
	global_atomic_add v4, v1, s[82:83]
	s_nop 0
	v_add_u32_e32 v4, 0x2000, v4
	global_atomic_add v4, v1, s[82:83]
	s_nop 0
	v_add_u32_e32 v4, 0x2000, v4
	global_atomic_add v4, v1, s[82:83]
	s_nop 0
	v_add_u32_e32 v4, 0x2000, v4
	global_atomic_add v4, v1, s[82:83]
	s_nop 0
	v_add_u32_e32 v4, 0x2000, v4
	global_atomic_add v4, v1, s[82:83]
	s_nop 0
	v_add_u32_e32 v4, 0x2000, v4
	global_atomic_add v4, v1, s[82:83]
	s_nop 0
	v_add_u32_e32 v4, 0x2000, v4
	global_atomic_add v4, v1, s[82:83]
	s_nop 0
	v_add_u32_e32 v4, 0x2000, v4
	global_atomic_add v4, v1, s[82:83]
	s_nop 0
	v_add_u32_e32 v4, 0x2000, v4
	global_atomic_add v4, v1, s[82:83]
	s_nop 0
	v_add_u32_e32 v4, 0x2000, v4
	global_atomic_add v4, v1, s[82:83]
	s_nop 0
	v_add_u32_e32 v4, 0x2000, v4
	global_atomic_add v4, v1, s[82:83]
	s_nop 0
	v_add_u32_e32 v4, 0x2000, v4
	global_atomic_add v4, v1, s[82:83]
	s_nop 0
	v_add_u32_e32 v4, 0x2000, v4
	global_atomic_add v4, v1, s[82:83]
	s_nop 0
	v_add_u32_e32 v4, 0x2000, v4
	global_atomic_add v4, v1, s[82:83]
	s_nop 0
	v_add_u32_e32 v4, 0x2000, v4
	global_atomic_add v4, v1, s[82:83]
	s_nop 0
	v_add_u32_e32 v4, 0x2000, v4
	global_atomic_add v4, v1, s[82:83]
.LBB0_1051:
	s_or_b64 exec, exec, s[10:11]
	s_mov_b64 s[10:11], exec
	v_mbcnt_lo_u32_b32 v1, s10, 0
	v_mbcnt_hi_u32_b32 v1, s11, v1
	v_cmp_eq_u32_e32 vcc, 0, v1
	s_and_saveexec_b64 s[12:13], vcc
	s_cbranch_execz .LBB0_1053
	s_bcnt1_i32_b64 s10, s[10:11]
	v_mov_b32_e32 v1, 0
	v_mov_b32_e32 v2, s10
	global_atomic_add v1, v2, s[100:101]

; __device__ __forceinline__ unsigned xb_ld(unsigned* p)              { return __hip_atomic_load(p, __ATOMIC_RELAXED, __HIP_MEMORY_SCOPE_AGENT); }
; __device__ __forceinline__ unsigned xb_add(unsigned* p, unsigned v) { return __hip_atomic_fetch_add(p, v, __ATOMIC_RELAXED, __HIP_MEMORY_SCOPE_AGENT); }
; #define XB_SPIN(cond, bar) do { unsigned _sp = 0; while (cond) { __builtin_amdgcn_s_sleep(1); \
;     if ((++_sp & 255u) == 0u) { if (xb_ld(&(bar)[XB_TMO])) break; if (_sp > XB_SPIN_CAP) { atomicAdd(&(bar)[XB_TMO], 1u); break; } } } } while (0)
; __device__ __forceinline__ void xcd_barrier(const XcdBarrier& b) {
;     ...
;         const unsigned old = xb_add(&bar[XB_XSUB(b.x)], 1u);
;         const unsigned gen = old / nloc;
;         if (old + 1u == (gen + 1u) * nloc) {
;             asm volatile("buffer_inv sc1" ::: "memory");
;             __builtin_amdgcn_fence(__ATOMIC_RELEASE, "agent");
;             asm volatile("s_waitcnt vmcnt(0)" ::: "memory");
;             const unsigned og = xb_add(&bar[XB_TOP], 1u);
;             const unsigned tg = og / nx;
;             if (og + 1u == (tg + 1u) * nx) xb_add(&bar[XB_TOPGEN], 1u);
;             else XB_SPIN(xb_ld(&bar[XB_TOPGEN]) == tg, bar);
;             asm volatile("" ::: "memory");
;             xb_add(&bar[XB_XGEN(b.x)], 1u);
;             asm volatile("" ::: "memory");
;         } else {
;             asm volatile("buffer_inv sc1" ::: "memory");
;             XB_SPIN(xb_ld(&bar[XB_XGEN(b.x)]) == gen, bar);
;             asm volatile("" ::: "memory");
;             asm volatile("s_waitcnt vmcnt(0)" ::: "memory");
.LBB0_1228:
	s_or_b64 exec, exec, s[14:15]
	v_cvt_f32_u32_e32 v5, v3
	s_waitcnt vmcnt(0)
	v_readfirstlane_b32 s12, v4
	v_sub_u32_e32 v4, 0, v3
	v_rcp_iflag_f32_e32 v5, v5
	v_add_u32_e32 v6, s12, v2
	v_mul_f32_e32 v5, 0x4f7ffffe, v5
	v_cvt_u32_f32_e32 v5, v5
	v_mul_lo_u32 v2, v4, v5
	v_mul_hi_u32 v2, v5, v2
	v_add_u32_e32 v2, v5, v2
	v_mul_hi_u32 v2, v6, v2
	v_mul_lo_u32 v4, v2, v3
	v_sub_u32_e32 v4, v6, v4
	v_add_u32_e32 v5, 1, v2
	v_cmp_ge_u32_e32 vcc, v4, v3
	s_nop 1
	v_cndmask_b32_e32 v2, v2, v5, vcc
	v_sub_u32_e32 v5, v4, v3
	v_cndmask_b32_e32 v4, v4, v5, vcc
	v_add_u32_e32 v5, 1, v2
	v_cmp_ge_u32_e32 vcc, v4, v3
	v_add_u32_e32 v4, 1, v6
	s_nop 0
	v_cndmask_b32_e32 v2, v2, v5, vcc
	v_mul_lo_u32 v5, v3, v2
	v_readfirstlane_b32 s98, v2
	v_readlane_b32 s100, v251, 6
	s_lshl_b32 s100, s100, 13
	s_add_u32 s100, s100, s82
	s_addc_u32 s101, s83, 0
	s_add_u32 s100, s100, 0x40000
	s_addc_u32 s101, s101, 0
	v_add_u32_e32 v3, v5, v3
	v_cmp_ne_u32_e32 vcc, v4, v3
	s_and_saveexec_b64 s[12:13], vcc
	s_xor_b64 s[12:13], exec, s[12:13]
	s_cbranch_execz .LBB0_1242
	buffer_inv sc1
	v_lshl_add_u32 v2, v2, 1, 1
	s_waitcnt lgkmcnt(0)
	v_mov_b32_e32 v1, 0
	global_load_dword v1, v1, s[100:101] sc1
	s_mov_b32 s18, s100
	s_mov_b32 s19, s101
	s_waitcnt vmcnt(0)
	v_cmp_lt_u32_e32 vcc, v1, v2
	s_and_saveexec_b64 s[14:15], vcc
	s_cbranch_execz .LBB0_1241
	s_add_u32 s16, s82, 0x4200
	s_addc_u32 s17, s83, 0
	s_mov_b32 s30, 1
	s_mov_b64 s[20:21], 0
	v_mov_b32_e32 v1, 0
	s_branch .LBB0_1232

; __device__ __forceinline__ unsigned xb_ld(unsigned* p)              { return __hip_atomic_load(p, __ATOMIC_RELAXED, __HIP_MEMORY_SCOPE_AGENT); }
; __device__ __forceinline__ unsigned xb_add(unsigned* p, unsigned v) { return __hip_atomic_fetch_add(p, v, __ATOMIC_RELAXED, __HIP_MEMORY_SCOPE_AGENT); }
; #define XB_SPIN(cond, bar) do { unsigned _sp = 0; while (cond) { __builtin_amdgcn_s_sleep(1); \
;     if ((++_sp & 255u) == 0u) { if (xb_ld(&(bar)[XB_TMO])) break; if (_sp > XB_SPIN_CAP) { atomicAdd(&(bar)[XB_TMO], 1u); break; } } } } while (0)
; __device__ __forceinline__ void xcd_barrier(const XcdBarrier& b) {
;     ...
;             const unsigned og = xb_add(&bar[XB_TOP], 1u);
;             const unsigned tg = og / nx;
;             if (og + 1u == (tg + 1u) * nx) xb_add(&bar[XB_TOPGEN], 1u);
;             else XB_SPIN(xb_ld(&bar[XB_TOPGEN]) == tg, bar);
.LBB0_1245:
	s_or_b64 exec, exec, s[14:15]
	v_cvt_f32_u32_e32 v4, v1
	s_waitcnt vmcnt(0)
	v_readfirstlane_b32 s12, v3
	s_add_u32 s14, s82, 0x7500
	s_addc_u32 s15, s83, 0
	v_rcp_iflag_f32_e32 v4, v4
	v_add_u32_e32 v2, s12, v2
	v_add_u32_e32 v5, 1, v2
	s_mov_b64 s[16:17], -1
	v_mul_f32_e32 v3, 0x4f7ffffe, v4
	v_cvt_u32_f32_e32 v3, v3
	v_sub_u32_e32 v4, 0, v1
	v_mul_lo_u32 v4, v4, v3
	v_mul_hi_u32 v4, v3, v4
	v_add_u32_e32 v3, v3, v4
	v_mul_hi_u32 v3, v2, v3
	v_mul_lo_u32 v4, v3, v1
	v_sub_u32_e32 v2, v2, v4
	v_add_u32_e32 v6, 1, v3
	v_cmp_ge_u32_e32 vcc, v2, v1
	v_sub_u32_e32 v4, v2, v1
	s_nop 0
	v_cndmask_b32_e32 v3, v3, v6, vcc
	v_cndmask_b32_e32 v2, v2, v4, vcc
	v_add_u32_e32 v4, 1, v3
	v_cmp_ge_u32_e32 vcc, v2, v1
	s_nop 1
	v_cndmask_b32_e32 v4, v3, v4, vcc
	v_mul_lo_u32 v2, v1, v4
	v_add_u32_e32 v1, v2, v1
	v_cmp_ne_u32_e32 vcc, v5, v1
	v_mov_b64_e32 v[2:3], s[14:15]
	s_and_saveexec_b64 s[12:13], vcc
	s_cbranch_execz .LBB0_1257
	s_mov_b32 s14, s100
	s_mov_b32 s15, s101
	v_mov_b32_e32 v4, s98
	v_lshl_add_u32 v4, v4, 1, 1
	v_mov_b32_e32 v1, 0
	global_load_dword v2, v1, s[14:15] sc1
	s_mov_b64 s[20:21], 0
	s_waitcnt vmcnt(0)
	v_cmp_lt_u32_e32 vcc, v2, v4
	s_and_saveexec_b64 s[18:19], vcc
	s_cbranch_execz .LBB0_1256
	s_add_u32 s16, s82, 0x4200
	s_addc_u32 s17, s83, 0
	s_mov_b32 s30, 1
	s_branch .LBB0_1249

; __device__ __forceinline__ unsigned xb_ld(unsigned* p)              { return __hip_atomic_load(p, __ATOMIC_RELAXED, __HIP_MEMORY_SCOPE_AGENT); }
; __device__ __forceinline__ unsigned xb_add(unsigned* p, unsigned v) { return __hip_atomic_fetch_add(p, v, __ATOMIC_RELAXED, __HIP_MEMORY_SCOPE_AGENT); }
; #define XB_SPIN(cond, bar) do { unsigned _sp = 0; while (cond) { __builtin_amdgcn_s_sleep(1); \
;     if ((++_sp & 255u) == 0u) { if (xb_ld(&(bar)[XB_TMO])) break; if (_sp > XB_SPIN_CAP) { atomicAdd(&(bar)[XB_TMO], 1u); break; } } } } while (0)
; __device__ __forceinline__ void xcd_barrier(const XcdBarrier& b) {
;     ...
;             if (og + 1u == (tg + 1u) * nx) xb_add(&bar[XB_TOPGEN], 1u);
;             else XB_SPIN(xb_ld(&bar[XB_TOPGEN]) == tg, bar);
;             asm volatile("" ::: "memory");
;             xb_add(&bar[XB_XGEN(b.x)], 1u);
;             asm volatile("" ::: "memory");
.LBB0_1257:
	s_or_b64 exec, exec, s[12:13]
	s_and_saveexec_b64 s[12:13], s[16:17]
	s_cbranch_execz .LBB0_1259
	v_mov_b32_e32 v1, 1
	global_atomic_add v[2:3], v1, off
	v_mov_b32_e32 v4, 0x40000
	global_atomic_add v4, v1, s[82:83]
	s_nop 0
	v_add_u32_e32 v4, 0x2000, v4
	global_atomic_add v4, v1, s[82:83]
	s_nop 0
	v_add_u32_e32 v4, 0x2000, v4
	global_atomic_add v4, v1, s[82:83]
	s_nop 0
	v_add_u32_e32 v4, 0x2000, v4
	global_atomic_add v4, v1, s[82:83]
	s_nop 0
	v_add_u32_e32 v4, 0x2000, v4
	global_atomic_add v4, v1, s[82:83]
	s_nop 0
	v_add_u32_e32 v4, 0x2000, v4
	global_atomic_add v4, v1, s[82:83]
	s_nop 0
	v_add_u32_e32 v4, 0x2000, v4
	global_atomic_add v4, v1, s[82:83]
	s_nop 0
	v_add_u32_e32 v4, 0x2000, v4
	global_atomic_add v4, v1, s[82:83]
	s_nop 0
	v_add_u32_e32 v4, 0x2000, v4
	global_atomic_add v4, v1, s[82:83]
	s_nop 0
	v_add_u32_e32 v4, 0x2000, v4
	global_atomic_add v4, v1, s[82:83]
	s_nop 0
	v_add_u32_e32 v4, 0x2000, v4
	global_atomic_add v4, v1, s[82:83]
	s_nop 0
	v_add_u32_e32 v4, 0x2000, v4
	global_atomic_add v4, v1, s[82:83]
	s_nop 0
	v_add_u32_e32 v4, 0x2000, v4
	global_atomic_add v4, v1, s[82:83]
	s_nop 0
	v_add_u32_e32 v4, 0x2000, v4
	global_atomic_add v4, v1, s[82:83]
	s_nop 0
	v_add_u32_e32 v4, 0x2000, v4
	global_atomic_add v4, v1, s[82:83]
	s_nop 0
	v_add_u32_e32 v4, 0x2000, v4
	global_atomic_add v4, v1, s[82:83]
.LBB0_1259:
	s_or_b64 exec, exec, s[12:13]
	s_mov_b64 s[12:13], exec
	v_mbcnt_lo_u32_b32 v1, s12, 0
	v_mbcnt_hi_u32_b32 v1, s13, v1
	v_cmp_eq_u32_e32 vcc, 0, v1
	s_and_saveexec_b64 s[14:15], vcc
	s_cbranch_execz .LBB0_1261
	s_bcnt1_i32_b64 s12, s[12:13]
	v_mov_b32_e32 v1, 0
	v_mov_b32_e32 v2, s12
	global_atomic_add v1, v2, s[100:101]

; __device__ __forceinline__ unsigned xb_ld(unsigned* p)              { return __hip_atomic_load(p, __ATOMIC_RELAXED, __HIP_MEMORY_SCOPE_AGENT); }
; __device__ __forceinline__ unsigned xb_add(unsigned* p, unsigned v) { return __hip_atomic_fetch_add(p, v, __ATOMIC_RELAXED, __HIP_MEMORY_SCOPE_AGENT); }
; #define XB_SPIN(cond, bar) do { unsigned _sp = 0; while (cond) { __builtin_amdgcn_s_sleep(1); \
;     if ((++_sp & 255u) == 0u) { if (xb_ld(&(bar)[XB_TMO])) break; if (_sp > XB_SPIN_CAP) { atomicAdd(&(bar)[XB_TMO], 1u); break; } } } } while (0)
; __device__ __forceinline__ void xcd_barrier(const XcdBarrier& b) {
;     ...
;         const unsigned old = xb_add(&bar[XB_XSUB(b.x)], 1u);
;         const unsigned gen = old / nloc;
;         if (old + 1u == (gen + 1u) * nloc) {
;             asm volatile("buffer_inv sc1" ::: "memory");
;             __builtin_amdgcn_fence(__ATOMIC_RELEASE, "agent");
;             asm volatile("s_waitcnt vmcnt(0)" ::: "memory");
;             const unsigned og = xb_add(&bar[XB_TOP], 1u);
;             const unsigned tg = og / nx;
;             if (og + 1u == (tg + 1u) * nx) xb_add(&bar[XB_TOPGEN], 1u);
;             else XB_SPIN(xb_ld(&bar[XB_TOPGEN]) == tg, bar);
;             asm volatile("" ::: "memory");
;             xb_add(&bar[XB_XGEN(b.x)], 1u);
;             asm volatile("" ::: "memory");
;         } else {
;             asm volatile("buffer_inv sc1" ::: "memory");
;             XB_SPIN(xb_ld(&bar[XB_XGEN(b.x)]) == gen, bar);
;             asm volatile("" ::: "memory");
;             asm volatile("s_waitcnt vmcnt(0)" ::: "memory");
.LBB0_1841:
	s_or_b64 exec, exec, s[12:13]
	v_cvt_f32_u32_e32 v5, v3
	s_waitcnt vmcnt(0)
	v_readfirstlane_b32 s3, v4
	v_sub_u32_e32 v4, 0, v3
	v_rcp_iflag_f32_e32 v5, v5
	v_add_u32_e32 v6, s3, v2
	v_mul_f32_e32 v5, 0x4f7ffffe, v5
	v_cvt_u32_f32_e32 v5, v5
	v_mul_lo_u32 v2, v4, v5
	v_mul_hi_u32 v2, v5, v2
	v_add_u32_e32 v2, v5, v2
	v_mul_hi_u32 v2, v6, v2
	v_mul_lo_u32 v4, v2, v3
	v_sub_u32_e32 v4, v6, v4
	v_add_u32_e32 v5, 1, v2
	v_cmp_ge_u32_e32 vcc, v4, v3
	s_nop 1
	v_cndmask_b32_e32 v2, v2, v5, vcc
	v_sub_u32_e32 v5, v4, v3
	v_cndmask_b32_e32 v4, v4, v5, vcc
	v_add_u32_e32 v5, 1, v2
	v_cmp_ge_u32_e32 vcc, v4, v3
	v_add_u32_e32 v4, 1, v6
	s_nop 0
	v_cndmask_b32_e32 v2, v2, v5, vcc
	v_mul_lo_u32 v5, v3, v2
	v_readfirstlane_b32 s98, v2
	v_readlane_b32 s100, v251, 6
	s_lshl_b32 s100, s100, 13
	s_add_u32 s100, s100, s82
	s_addc_u32 s101, s83, 0
	s_add_u32 s100, s100, 0x40000
	s_addc_u32 s101, s101, 0
	v_add_u32_e32 v3, v5, v3
	v_cmp_ne_u32_e32 vcc, v4, v3
	s_and_saveexec_b64 s[10:11], vcc
	s_xor_b64 s[10:11], exec, s[10:11]
	s_cbranch_execz .LBB0_1855
	buffer_inv sc1
	v_lshl_add_u32 v2, v2, 1, 1
	s_waitcnt lgkmcnt(0)
	v_mov_b32_e32 v1, 0
	global_load_dword v1, v1, s[100:101] sc1
	s_mov_b32 s16, s100
	s_mov_b32 s17, s101
	s_waitcnt vmcnt(0)
	v_cmp_lt_u32_e32 vcc, v1, v2
	s_and_saveexec_b64 s[12:13], vcc
	s_cbranch_execz .LBB0_1854
	s_add_u32 s14, s82, 0x4200
	s_addc_u32 s15, s83, 0
	s_mov_b32 s3, 1
	s_mov_b64 s[18:19], 0
	v_mov_b32_e32 v1, 0
	s_branch .LBB0_1845

; __device__ __forceinline__ unsigned xb_ld(unsigned* p)              { return __hip_atomic_load(p, __ATOMIC_RELAXED, __HIP_MEMORY_SCOPE_AGENT); }
; __device__ __forceinline__ unsigned xb_add(unsigned* p, unsigned v) { return __hip_atomic_fetch_add(p, v, __ATOMIC_RELAXED, __HIP_MEMORY_SCOPE_AGENT); }
; #define XB_SPIN(cond, bar) do { unsigned _sp = 0; while (cond) { __builtin_amdgcn_s_sleep(1); \
;     if ((++_sp & 255u) == 0u) { if (xb_ld(&(bar)[XB_TMO])) break; if (_sp > XB_SPIN_CAP) { atomicAdd(&(bar)[XB_TMO], 1u); break; } } } } while (0)
; __device__ __forceinline__ void xcd_barrier(const XcdBarrier& b) {
;     ...
;             const unsigned og = xb_add(&bar[XB_TOP], 1u);
;             const unsigned tg = og / nx;
;             if (og + 1u == (tg + 1u) * nx) xb_add(&bar[XB_TOPGEN], 1u);
;             else XB_SPIN(xb_ld(&bar[XB_TOPGEN]) == tg, bar);
.LBB0_1858:
	s_or_b64 exec, exec, s[12:13]
	v_cvt_f32_u32_e32 v4, v1
	s_waitcnt vmcnt(0)
	v_readfirstlane_b32 s3, v3
	s_add_u32 s12, s82, 0x7500
	s_addc_u32 s13, s83, 0
	v_rcp_iflag_f32_e32 v4, v4
	v_add_u32_e32 v2, s3, v2
	v_add_u32_e32 v5, 1, v2
	s_mov_b64 s[14:15], -1
	v_mul_f32_e32 v3, 0x4f7ffffe, v4
	v_cvt_u32_f32_e32 v3, v3
	v_sub_u32_e32 v4, 0, v1
	v_mul_lo_u32 v4, v4, v3
	v_mul_hi_u32 v4, v3, v4
	v_add_u32_e32 v3, v3, v4
	v_mul_hi_u32 v3, v2, v3
	v_mul_lo_u32 v4, v3, v1
	v_sub_u32_e32 v2, v2, v4
	v_add_u32_e32 v6, 1, v3
	v_cmp_ge_u32_e32 vcc, v2, v1
	v_sub_u32_e32 v4, v2, v1
	s_nop 0
	v_cndmask_b32_e32 v3, v3, v6, vcc
	v_cndmask_b32_e32 v2, v2, v4, vcc
	v_add_u32_e32 v4, 1, v3
	v_cmp_ge_u32_e32 vcc, v2, v1
	s_nop 1
	v_cndmask_b32_e32 v4, v3, v4, vcc
	v_mul_lo_u32 v2, v1, v4
	v_add_u32_e32 v1, v2, v1
	v_cmp_ne_u32_e32 vcc, v5, v1
	v_mov_b64_e32 v[2:3], s[12:13]
	s_and_saveexec_b64 s[10:11], vcc
	s_cbranch_execz .LBB0_1870
	s_mov_b32 s12, s100
	s_mov_b32 s13, s101
	v_mov_b32_e32 v4, s98
	v_lshl_add_u32 v4, v4, 1, 1
	v_mov_b32_e32 v1, 0
	global_load_dword v2, v1, s[12:13] sc1
	s_mov_b64 s[18:19], 0
	s_waitcnt vmcnt(0)
	v_cmp_lt_u32_e32 vcc, v2, v4
	s_and_saveexec_b64 s[16:17], vcc
	s_cbranch_execz .LBB0_1869
	s_add_u32 s14, s82, 0x4200
	s_addc_u32 s15, s83, 0
	s_mov_b32 s3, 1
	s_branch .LBB0_1862

; __device__ __forceinline__ unsigned xb_ld(unsigned* p)              { return __hip_atomic_load(p, __ATOMIC_RELAXED, __HIP_MEMORY_SCOPE_AGENT); }
; __device__ __forceinline__ unsigned xb_add(unsigned* p, unsigned v) { return __hip_atomic_fetch_add(p, v, __ATOMIC_RELAXED, __HIP_MEMORY_SCOPE_AGENT); }
; #define XB_SPIN(cond, bar) do { unsigned _sp = 0; while (cond) { __builtin_amdgcn_s_sleep(1); \
;     if ((++_sp & 255u) == 0u) { if (xb_ld(&(bar)[XB_TMO])) break; if (_sp > XB_SPIN_CAP) { atomicAdd(&(bar)[XB_TMO], 1u); break; } } } } while (0)
; __device__ __forceinline__ void xcd_barrier(const XcdBarrier& b) {
;     ...
;             if (og + 1u == (tg + 1u) * nx) xb_add(&bar[XB_TOPGEN], 1u);
;             else XB_SPIN(xb_ld(&bar[XB_TOPGEN]) == tg, bar);
;             asm volatile("" ::: "memory");
;             xb_add(&bar[XB_XGEN(b.x)], 1u);
;             asm volatile("" ::: "memory");
.LBB0_1872:
	s_or_b64 exec, exec, s[10:11]
	s_mov_b64 s[10:11], exec
	v_mbcnt_lo_u32_b32 v1, s10, 0
	v_mbcnt_hi_u32_b32 v1, s11, v1
	v_cmp_eq_u32_e32 vcc, 0, v1
	s_and_saveexec_b64 s[12:13], vcc
	s_cbranch_execz .LBB0_1874
	s_bcnt1_i32_b64 s3, s[10:11]
	v_mov_b32_e32 v1, 0
	v_mov_b32_e32 v2, s3
	global_atomic_add v1, v2, s[100:101]

; #define LAS __attribute__((address_space(3)))
; __global__ void __launch_bounds__(512, 2) dit_fwd(Args args) {
;     extern __shared__ __attribute__((aligned(16))) unsigned char lds_raw[];
;     LAS unsigned char* lds = (LAS unsigned char*)lds_raw;
	.amdhsa_kernel _Z7dit_fwd4Args
		.amdhsa_group_segment_fixed_size 0
		.amdhsa_private_segment_fixed_size 0
		.amdhsa_kernarg_size 440
		.amdhsa_user_sgpr_count 2
		.amdhsa_user_sgpr_dispatch_ptr 0
		.amdhsa_user_sgpr_queue_ptr 0
		.amdhsa_user_sgpr_kernarg_segment_ptr 1
		.amdhsa_user_sgpr_dispatch_id 0
		.amdhsa_user_sgpr_kernarg_preload_length 0
		.amdhsa_user_sgpr_kernarg_preload_offset 0
		.amdhsa_user_sgpr_private_segment_size 0
		.amdhsa_uses_dynamic_stack 0
		.amdhsa_enable_private_segment 0
		.amdhsa_system_sgpr_workgroup_id_x 1
		.amdhsa_system_sgpr_workgroup_id_y 0
		.amdhsa_system_sgpr_workgroup_id_z 0
		.amdhsa_system_sgpr_workgroup_info 0
		.amdhsa_system_vgpr_workitem_id 0
		.amdhsa_next_free_vgpr 252
		.amdhsa_next_free_sgpr 102
		.amdhsa_accum_offset 252
		.amdhsa_reserve_vcc 1
		.amdhsa_float_round_mode_32 0
		.amdhsa_float_round_mode_16_64 0
		.amdhsa_float_denorm_mode_32 3
		.amdhsa_float_denorm_mode_16_64 3
		.amdhsa_dx10_clamp 1
		.amdhsa_ieee_mode 1
		.amdhsa_fp16_overflow 0
		.amdhsa_tg_split 0
		.amdhsa_exception_fp_ieee_invalid_op 0
		.amdhsa_exception_fp_denorm_src 0
		.amdhsa_exception_fp_ieee_div_zero 0
		.amdhsa_exception_fp_ieee_overflow 0
		.amdhsa_exception_fp_ieee_underflow 0
		.amdhsa_exception_fp_ieee_inexact 0
		.amdhsa_exception_int_div_zero 0
	.end_amdhsa_kernel

; #define LAS __attribute__((address_space(3)))
; __global__ void __launch_bounds__(512, 2) dit_fwd(Args args) {
;     extern __shared__ __attribute__((aligned(16))) unsigned char lds_raw[];
;     LAS unsigned char* lds = (LAS unsigned char*)lds_raw;
amdhsa.kernels:
  - .agpr_count:     0
    .args:
      - .offset:         0
        .size:           184
        .value_kind:     by_value
      - .offset:         184
        .size:           4
        .value_kind:     hidden_block_count_x
      - .offset:         188
        .size:           4
        .value_kind:     hidden_block_count_y
      - .offset:         192
        .size:           4
        .value_kind:     hidden_block_count_z
      - .offset:         196
        .size:           2
        .value_kind:     hidden_group_size_x
      - .offset:         198
        .size:           2
        .value_kind:     hidden_group_size_y
      - .offset:         200
        .size:           2
        .value_kind:     hidden_group_size_z
      - .offset:         202
        .size:           2
        .value_kind:     hidden_remainder_x
      - .offset:         204
        .size:           2
        .value_kind:     hidden_remainder_y
      - .offset:         206
        .size:           2
        .value_kind:     hidden_remainder_z
      - .offset:         224
        .size:           8
        .value_kind:     hidden_global_offset_x
      - .offset:         232
        .size:           8
        .value_kind:     hidden_global_offset_y
      - .offset:         240
        .size:           8
        .value_kind:     hidden_global_offset_z
      - .offset:         248
        .size:           2
        .value_kind:     hidden_grid_dims
      - .offset:         304
        .size:           4
        .value_kind:     hidden_dynamic_lds_size
    .group_segment_fixed_size: 0
    .kernarg_segment_align: 8
    .kernarg_segment_size: 440
    .language:       OpenCL C
    .language_version:
      - 2
      - 0
    .max_flat_workgroup_size: 512
    .name:           _Z7dit_fwd4Args
    .private_segment_fixed_size: 0
    .sgpr_count:     108
    .sgpr_spill_count: 107
    .symbol:         _Z7dit_fwd4Args.kd
    .uniform_work_group_size: 1
    .uses_dynamic_stack: false
    .vgpr_count:     252
    .vgpr_spill_count: 0
    .wavefront_size: 64
